# v89 + k3 head-norm row-sum exchange: dropped the L1 invalidate after the partner poll (the partner's sums are read with agent-scope sc1 loads that bypass L1; nothing else read afterwards was produced
# speedup vs baseline: 1.0276x; 1.0026x over previous
.LBB0_837:
	s_and_b64 exec, exec, s[42:43]
	s_add_i32 s8, 0, 0x27000
	v_cndmask_b32_e64 v134, 0, 1, s[68:69]
	v_mov_b32_e32 v135, s8
	ds_write_b32 v135, v134
